# baseline (speedup 1.0000x reference)
.Lk1_flush:
	s_barrier
	s_add_u32 s20, s40, 0x0
	s_addc_u32 s21, s41, 0
	s_add_u32 s22, s20, 0x186a000
	s_addc_u32 s23, s21, 0
	s_add_u32 s24, s22, 0x186a000
	s_addc_u32 s25, s23, 0
	s_add_u32 s26, s24, 0x186a000
	s_addc_u32 s27, s25, 0
	global_store_dword v39, v56, s[20:21] sc1
	global_store_dword v39, v57, s[22:23] sc1
	global_store_dword v39, v58, s[24:25] sc1
	global_store_dword v39, v59, s[26:27] sc1
	s_add_u32 s20, s20, 0x80000
	s_addc_u32 s21, s21, 0
	s_add_u32 s22, s22, 0x80000
	s_addc_u32 s23, s23, 0
	s_add_u32 s24, s24, 0x80000
	s_addc_u32 s25, s25, 0
	s_add_u32 s26, s26, 0x80000
	s_addc_u32 s27, s27, 0
	global_store_dword v39, v60, s[20:21] sc1
	global_store_dword v39, v61, s[22:23] sc1
	global_store_dword v39, v62, s[24:25] sc1
	global_store_dword v39, v63, s[26:27] sc1
	s_add_u32 s20, s20, 0x80000
	s_addc_u32 s21, s21, 0
	s_add_u32 s22, s22, 0x80000
	s_addc_u32 s23, s23, 0
	s_add_u32 s24, s24, 0x80000
	s_addc_u32 s25, s25, 0
	s_add_u32 s26, s26, 0x80000
	s_addc_u32 s27, s27, 0
	global_store_dword v39, v64, s[20:21] sc1
	global_store_dword v39, v65, s[22:23] sc1
	global_store_dword v39, v66, s[24:25] sc1
	global_store_dword v39, v67, s[26:27] sc1
	s_add_u32 s20, s20, 0x80000
	s_addc_u32 s21, s21, 0
	s_add_u32 s22, s22, 0x80000
	s_addc_u32 s23, s23, 0
	s_add_u32 s24, s24, 0x80000
	s_addc_u32 s25, s25, 0
	s_add_u32 s26, s26, 0x80000
	s_addc_u32 s27, s27, 0
	global_store_dword v39, v68, s[20:21] sc1
	global_store_dword v39, v69, s[22:23] sc1
	global_store_dword v39, v70, s[24:25] sc1
	global_store_dword v39, v71, s[26:27] sc1
	s_add_u32 s20, s20, 0x80000
	s_addc_u32 s21, s21, 0
	s_add_u32 s22, s22, 0x80000
	s_addc_u32 s23, s23, 0
	s_add_u32 s24, s24, 0x80000
	s_addc_u32 s25, s25, 0
	s_add_u32 s26, s26, 0x80000
	s_addc_u32 s27, s27, 0
	global_store_dword v39, v72, s[20:21] sc1
	global_store_dword v39, v73, s[22:23] sc1
	global_store_dword v39, v74, s[24:25] sc1
	global_store_dword v39, v75, s[26:27] sc1
	s_add_u32 s20, s20, 0x80000
	s_addc_u32 s21, s21, 0
	s_add_u32 s22, s22, 0x80000
	s_addc_u32 s23, s23, 0
	s_add_u32 s24, s24, 0x80000
	s_addc_u32 s25, s25, 0
	s_add_u32 s26, s26, 0x80000
	s_addc_u32 s27, s27, 0
	global_store_dword v39, v76, s[20:21] sc1
	global_store_dword v39, v77, s[22:23] sc1
	global_store_dword v39, v78, s[24:25] sc1
	global_store_dword v39, v79, s[26:27] sc1
	s_add_u32 s20, s20, 0x80000
	s_addc_u32 s21, s21, 0
	s_add_u32 s22, s22, 0x80000
	s_addc_u32 s23, s23, 0
	s_add_u32 s24, s24, 0x80000
	s_addc_u32 s25, s25, 0
	s_add_u32 s26, s26, 0x80000
	s_addc_u32 s27, s27, 0
	global_store_dword v39, v80, s[20:21] sc1
	global_store_dword v39, v81, s[22:23] sc1
	global_store_dword v39, v82, s[24:25] sc1
	global_store_dword v39, v83, s[26:27] sc1
	s_add_u32 s20, s20, 0x80000
	s_addc_u32 s21, s21, 0
	s_add_u32 s22, s22, 0x80000
	s_addc_u32 s23, s23, 0
	s_add_u32 s24, s24, 0x80000
	s_addc_u32 s25, s25, 0
	s_add_u32 s26, s26, 0x80000
	s_addc_u32 s27, s27, 0
	global_store_dword v39, v84, s[20:21] sc1
	global_store_dword v39, v85, s[22:23] sc1
	global_store_dword v39, v86, s[24:25] sc1
	global_store_dword v39, v87, s[26:27] sc1
	s_add_u32 s20, s20, 0x80000
	s_addc_u32 s21, s21, 0
	s_add_u32 s22, s22, 0x80000
	s_addc_u32 s23, s23, 0
	s_add_u32 s24, s24, 0x80000
	s_addc_u32 s25, s25, 0
	s_add_u32 s26, s26, 0x80000
	s_addc_u32 s27, s27, 0
	global_store_dword v39, v88, s[20:21] sc1
	global_store_dword v39, v89, s[22:23] sc1
	global_store_dword v39, v90, s[24:25] sc1
	global_store_dword v39, v91, s[26:27] sc1
	s_add_u32 s20, s20, 0x80000
	s_addc_u32 s21, s21, 0
	s_add_u32 s22, s22, 0x80000
	s_addc_u32 s23, s23, 0
	s_add_u32 s24, s24, 0x80000
	s_addc_u32 s25, s25, 0
	s_add_u32 s26, s26, 0x80000
	s_addc_u32 s27, s27, 0
	global_store_dword v39, v92, s[20:21] sc1
	global_store_dword v39, v93, s[22:23] sc1
	global_store_dword v39, v94, s[24:25] sc1
	global_store_dword v39, v95, s[26:27] sc1
	s_add_u32 s20, s20, 0x80000
	s_addc_u32 s21, s21, 0
	s_add_u32 s22, s22, 0x80000
	s_addc_u32 s23, s23, 0
	s_add_u32 s24, s24, 0x80000
	s_addc_u32 s25, s25, 0
	s_add_u32 s26, s26, 0x80000
	s_addc_u32 s27, s27, 0
	global_store_dword v39, v96, s[20:21] sc1
	global_store_dword v39, v97, s[22:23] sc1
	global_store_dword v39, v98, s[24:25] sc1
	global_store_dword v39, v99, s[26:27] sc1
	s_add_u32 s20, s20, 0x80000
	s_addc_u32 s21, s21, 0
	s_add_u32 s22, s22, 0x80000
	s_addc_u32 s23, s23, 0
	s_add_u32 s24, s24, 0x80000
	s_addc_u32 s25, s25, 0
	s_add_u32 s26, s26, 0x80000
	s_addc_u32 s27, s27, 0
	global_store_dword v39, v100, s[20:21] sc1
	global_store_dword v39, v101, s[22:23] sc1
	global_store_dword v39, v102, s[24:25] sc1
	global_store_dword v39, v103, s[26:27] sc1
	s_add_u32 s20, s20, 0x80000
	s_addc_u32 s21, s21, 0
	s_add_u32 s22, s22, 0x80000
	s_addc_u32 s23, s23, 0
	s_add_u32 s24, s24, 0x80000
	s_addc_u32 s25, s25, 0
	s_add_u32 s26, s26, 0x80000
	s_addc_u32 s27, s27, 0
	global_store_dword v39, v104, s[20:21] sc1
	global_store_dword v39, v105, s[22:23] sc1
	global_store_dword v39, v106, s[24:25] sc1
	global_store_dword v39, v107, s[26:27] sc1
	s_add_u32 s20, s20, 0x80000
	s_addc_u32 s21, s21, 0
	s_add_u32 s22, s22, 0x80000
	s_addc_u32 s23, s23, 0
	s_add_u32 s24, s24, 0x80000
	s_addc_u32 s25, s25, 0
	s_add_u32 s26, s26, 0x80000
	s_addc_u32 s27, s27, 0
	global_store_dword v39, v108, s[20:21] sc1
	global_store_dword v39, v109, s[22:23] sc1
	global_store_dword v39, v110, s[24:25] sc1
	global_store_dword v39, v111, s[26:27] sc1
	s_add_u32 s20, s20, 0x80000
	s_addc_u32 s21, s21, 0
	s_add_u32 s22, s22, 0x80000
	s_addc_u32 s23, s23, 0
	s_add_u32 s24, s24, 0x80000
	s_addc_u32 s25, s25, 0
	s_add_u32 s26, s26, 0x80000
	s_addc_u32 s27, s27, 0
	global_store_dword v39, v112, s[20:21] sc1
	global_store_dword v39, v113, s[22:23] sc1
	global_store_dword v39, v114, s[24:25] sc1
	global_store_dword v39, v115, s[26:27] sc1
	s_add_u32 s20, s20, 0x80000
	s_addc_u32 s21, s21, 0
	s_add_u32 s22, s22, 0x80000
	s_addc_u32 s23, s23, 0
	s_add_u32 s24, s24, 0x80000
	s_addc_u32 s25, s25, 0
	s_add_u32 s26, s26, 0x80000
	s_addc_u32 s27, s27, 0
	global_store_dword v39, v116, s[20:21] sc1
	global_store_dword v39, v117, s[22:23] sc1
	global_store_dword v39, v118, s[24:25] sc1
	global_store_dword v39, v119, s[26:27] sc1
	s_add_u32 s20, s20, 0x80000
	s_addc_u32 s21, s21, 0
	s_add_u32 s22, s22, 0x80000
	s_addc_u32 s23, s23, 0
	s_add_u32 s24, s24, 0x80000
	s_addc_u32 s25, s25, 0
	s_add_u32 s26, s26, 0x80000
	s_addc_u32 s27, s27, 0
	global_store_dword v39, v120, s[20:21] sc1
	global_store_dword v39, v121, s[22:23] sc1
	global_store_dword v39, v122, s[24:25] sc1
	global_store_dword v39, v123, s[26:27] sc1
	s_add_u32 s20, s20, 0x80000
	s_addc_u32 s21, s21, 0
	s_add_u32 s22, s22, 0x80000
	s_addc_u32 s23, s23, 0
	s_add_u32 s24, s24, 0x80000
	s_addc_u32 s25, s25, 0
	s_add_u32 s26, s26, 0x80000
	s_addc_u32 s27, s27, 0
	global_store_dword v39, v124, s[20:21] sc1
	global_store_dword v39, v125, s[22:23] sc1
	global_store_dword v39, v126, s[24:25] sc1
	global_store_dword v39, v127, s[26:27] sc1
	s_add_u32 s20, s20, 0x80000
	s_addc_u32 s21, s21, 0
	s_add_u32 s22, s22, 0x80000
	s_addc_u32 s23, s23, 0
	s_add_u32 s24, s24, 0x80000
	s_addc_u32 s25, s25, 0
	s_add_u32 s26, s26, 0x80000
	s_addc_u32 s27, s27, 0
	global_store_dword v39, v36, s[20:21] sc1
	global_store_dword v39, v37, s[22:23] sc1
	global_store_dword v39, v45, s[24:25] sc1
	global_store_dword v39, v46, s[26:27] sc1
	s_add_u32 s20, s20, 0x80000
	s_addc_u32 s21, s21, 0
	s_add_u32 s22, s22, 0x80000
	s_addc_u32 s23, s23, 0
	s_add_u32 s24, s24, 0x80000
	s_addc_u32 s25, s25, 0
	s_add_u32 s26, s26, 0x80000
	s_addc_u32 s27, s27, 0
	global_store_dword v39, v53, s[20:21] sc1
	global_store_dword v39, v54, s[22:23] sc1
	global_store_dword v39, v55, s[24:25] sc1
	global_store_dword v39, v1, s[26:27] sc1
	v_mul_f32_e32 v40, 0x3c010204, v40
	v_and_b32_e32 v42, 63, v0
	v_lshlrev_b32_e32 v41, 14, v42
	s_mov_b32 s15, s12
	s_lshl_b32 s15, s15, 2
	s_add_u32 s8, s8, s15
	s_addc_u32 s9, s9, 0
	s_add_u32 s15, s29, 24
	v_cmp_gt_u32_e32 vcc, s15, v42
	s_and_saveexec_b64 s[38:39], vcc
	global_store_dword v41, v40, s[8:9]
	s_mov_b64 exec, s[38:39]
	s_lshl_b32 s15, s14, 12
	v_add_u32_e32 v41, s15, v34
	s_barrier
	ds_write_b128 v41, v[2:5]
	ds_write_b128 v41, v[6:9] offset:1024
	ds_write_b128 v41, v[10:13] offset:2048
	ds_write_b128 v41, v[14:17] offset:3072
	s_waitcnt lgkmcnt(0)
	s_barrier
	s_movk_i32 s15, 0x100
	v_cmp_gt_u32_e32 vcc, s15, v0
	s_and_saveexec_b64 s[38:39], vcc
	s_cbranch_execz .Lk1_end
	v_lshlrev_b32_e32 v16, 4, v0
	ds_read_b128 v[2:5], v16
	ds_read_b128 v[18:21], v16 offset:4096
	ds_read_b128 v[22:25], v16 offset:8192
	ds_read_b128 v[26:29], v16 offset:12288
	ds_read_b128 v[30:33], v16 offset:16384
	ds_read_b128 v[34:37], v16 offset:20480
	ds_read_b128 v[38:41], v16 offset:24576
	ds_read_b128 v[42:45], v16 offset:28672
	s_waitcnt lgkmcnt(6)
	v_pk_add_f32 v[2:3], v[2:3], v[18:19]
	v_pk_add_f32 v[4:5], v[4:5], v[20:21]
	s_waitcnt lgkmcnt(5)
	v_pk_add_f32 v[2:3], v[2:3], v[22:23]
	v_pk_add_f32 v[4:5], v[4:5], v[24:25]
	s_waitcnt lgkmcnt(4)
	v_pk_add_f32 v[2:3], v[2:3], v[26:27]
	v_pk_add_f32 v[4:5], v[4:5], v[28:29]
	s_waitcnt lgkmcnt(3)
	v_pk_add_f32 v[2:3], v[2:3], v[30:31]
	v_pk_add_f32 v[4:5], v[4:5], v[32:33]
	s_waitcnt lgkmcnt(2)
	v_pk_add_f32 v[2:3], v[2:3], v[34:35]
	v_pk_add_f32 v[4:5], v[4:5], v[36:37]
	s_waitcnt lgkmcnt(1)
	v_pk_add_f32 v[2:3], v[2:3], v[38:39]
	v_pk_add_f32 v[4:5], v[4:5], v[40:41]
	s_waitcnt lgkmcnt(0)
	v_pk_add_f32 v[2:3], v[2:3], v[42:43]
	v_pk_add_f32 v[4:5], v[4:5], v[44:45]
	s_lshl_b32 s15, s2, 12
	s_add_u32 s10, s10, s15
	s_addc_u32 s11, s11, 0
	global_store_dwordx4 v16, v[2:5], s[10:11]
